# S2: hand-written consumer tile bodies (scalar B ptr, counters) + rowsum via mfma16x16x32 instead of dot2c
# baseline (speedup 1.0000x reference)
_Z11attn_kernelPKiPKDv8_DF16_PKDF16_S5_PDF16_Pf:
	s_mul_i32 s3, s2, 27
	s_mul_hi_i32 s26, s3, 0x2aaaaaab
	v_and_b32_e32 v102, 63, v0
	s_lshr_b32 s27, s26, 31
	s_ashr_i32 s28, s26, 3
	s_movk_i32 s4, 0x200
	v_lshrrev_b32_e32 v98, 6, v0
	s_add_i32 s28, s28, s27
	v_cmp_gt_u32_e32 vcc, s4, v0
	s_mul_hi_i32 s29, s3, 0x38e38e39
	v_lshlrev_b32_e32 v122, 4, v102
	s_and_saveexec_b64 s[4:5], vcc
	s_xor_b64 s[12:13], exec, s[4:5]
	s_cbranch_execz .LBB1_65
	s_lshr_b32 s6, s29, 31
	s_ashr_i32 s7, s29, 9
	s_add_i32 s6, s7, s6
	s_mul_i32 s7, s6, 0xffffffd0
	v_bfe_u32 v117, v0, 6, 2
	s_add_i32 s7, s7, s28
	v_lshl_or_b32 v4, s6, 2, v117
	s_lshl_b32 s6, s7, 6
	s_load_dwordx2 s[4:5], s[0:1], 0x8
	s_load_dwordx4 s[8:11], s[0:1], 0x18
	s_load_dwordx2 s[14:15], s[0:1], 0x28
	s_movk_i32 s30, 0xc00
	v_mov_b32_e32 v2, s6
	v_and_b32_e32 v119, 31, v0
	v_mad_i32_i24 v2, v4, s30, v2
	v_or_b32_e32 v2, v2, v119
	s_mul_i32 s6, s28, 48
	v_ashrrev_i32_e32 v3, 31, v2
	s_sub_i32 s6, s3, s6
	s_waitcnt lgkmcnt(0)
	v_lshl_add_u64 v[2:3], v[2:3], 1, s[8:9]
	s_lshl_b32 s6, s6, 2
	global_load_ushort v5, v[2:3], off
	global_load_ushort v6, v[2:3], off offset:64
	s_movk_i32 s31, 0xc0
	v_mov_b32_e32 v2, s6
	s_add_i32 s6, s3, 1
	v_mad_i32_i24 v2, v4, s31, v2
	v_lshrrev_b32_e32 v4, 7, v0
	s_mul_hi_i32 s7, s6, 0x2aaaaaab
	v_and_b32_e32 v121, 2, v4
	s_lshr_b32 s16, s7, 31
	s_lshr_b32 s7, s7, 3
	v_or_b32_e32 v2, v2, v121
	s_add_i32 s7, s7, s16
	v_ashrrev_i32_e32 v3, 31, v2
	s_mul_i32 s7, s7, 48
	v_lshlrev_b64 v[2:3], 11, v[2:3]
	s_sub_i32 s7, s6, s7
	s_mul_hi_i32 s6, s6, 0x38e38e39
	v_lshl_add_u64 v[2:3], s[4:5], 0, v[2:3]
	v_mov_b32_e32 v123, 0
	s_lshr_b32 s16, s6, 31
	s_lshr_b32 s6, s6, 9
	v_lshl_add_u64 v[2:3], v[2:3], 0, v[122:123]
	s_add_i32 s6, s6, s16
	global_load_dwordx4 v[86:89], v[2:3], off
	global_load_dwordx4 v[82:85], v[2:3], off offset:1024
	global_load_dwordx4 v[70:73], v[2:3], off offset:2048
	global_load_dwordx4 v[66:69], v[2:3], off offset:3072
	v_lshl_or_b32 v2, s6, 2, v117
	s_lshl_b32 s6, s7, 2
	v_mov_b32_e32 v3, s6
	v_mad_i32_i24 v2, v2, s31, v3
	v_or_b32_e32 v2, v2, v121
	v_ashrrev_i32_e32 v3, 31, v2
	v_lshlrev_b64 v[2:3], 11, v[2:3]
	v_lshl_add_u64 v[2:3], s[4:5], 0, v[2:3]
	v_lshl_add_u64 v[2:3], v[2:3], 0, v[122:123]
	global_load_dwordx4 v[94:97], v[2:3], off
	global_load_dwordx4 v[90:93], v[2:3], off offset:1024
	global_load_dwordx4 v[78:81], v[2:3], off offset:2048
	global_load_dwordx4 v[74:77], v[2:3], off offset:3072
	v_lshlrev_b32_e32 v3, 2, v102
	v_lshrrev_b32_e32 v1, 5, v102
	v_lshl_add_u64 v[114:115], s[4:5], 0, v[122:123]
	s_movk_i32 s4, 0xff
	v_lshl_or_b32 v127, v117, 14, v3
	v_lshlrev_b32_e32 v3, 8, v117
	v_lshlrev_b32_e32 v7, 2, v119
	s_mov_b32 s16, 0x15000
	v_cmp_lt_u32_e64 s[6:7], s4, v0
	v_or3_b32 v128, v3, v7, s16
	v_lshlrev_b32_e32 v3, 10, v1
	v_and_b32_e32 v0, 0xc0, v0
	v_lshlrev_b32_e32 v2, 1, v117
	v_or3_b32 v124, v3, v0, v119
	v_lshlrev_b32_e32 v0, 3, v121
	v_or3_b32 v0, v2, v0, v1
	v_lshlrev_b32_e32 v8, 6, v117
	v_lshlrev_b32_e32 v129, 5, v0
	v_or_b32_e32 v0, 1, v4
	v_or3_b32 v116, v3, v8, v119
	v_lshlrev_b32_e32 v3, 3, v0
	v_lshlrev_b32_e32 v125, 4, v1
	s_movk_i32 s16, 0x80
	v_or3_b32 v1, v2, v3, v1
	v_lshlrev_b32_e32 v133, 5, v0
	s_mov_b32 s36, 0x5040100
	v_mbcnt_lo_u32_b32 v0, -1, 0
	s_add_i32 s33, s3, 2
	v_cmp_gt_u32_e64 s[4:5], 32, v102
	s_lshl_b32 s34, s2, 1
	s_movk_i32 s35, 0x2000
	v_or_b32_e32 v118, 0x2000, v116
	v_or3_b32 v120, v7, v117, s16
	v_add_u32_e32 v126, v7, v98
	v_lshlrev_b32_e32 v130, 5, v121
	v_mul_u32_u24_e32 v131, 0x90, v119
	v_lshlrev_b32_e32 v132, 5, v1
	s_mov_b32 s42, 0
	s_movk_i32 s37, 0x5000
	s_movk_i32 s38, 0x6000
	s_movk_i32 s39, 0x7000
	s_movk_i32 s40, 0x1000
	s_movk_i32 s41, 0x3000
	v_mbcnt_hi_u32_b32 v134, -1, v0
	v_mov_b32_e32 v1, 0
	s_waitcnt vmcnt(9)
	v_perm_b32 v136, v5, v5, s36
	s_waitcnt vmcnt(8)
	v_perm_b32 v135, v6, v6, s36
	v_mov_b32_e32 v122, 0
	v_mov_b32_e32 v18, v123
	v_mov_b32_e32 v19, v123
	v_mov_b32_e32 v20, v123
	v_mov_b32_e32 v21, v123
	v_mov_b32_e32 v22, v123
	v_mov_b32_e32 v23, v123
	v_mov_b32_e32 v24, v123
	v_mov_b32_e32 v25, v123
	v_mov_b32_e32 v26, v123
	v_mov_b32_e32 v27, v123
	v_mov_b32_e32 v28, v123
	v_mov_b32_e32 v29, v123
	v_mov_b32_e32 v30, v123
	v_mov_b32_e32 v31, v123
	v_mov_b32_e32 v32, v123
	v_mov_b32_e32 v33, v123
	v_mov_b32_e32 v50, v123
	v_mov_b32_e32 v51, v123
	v_mov_b32_e32 v52, v123
	v_mov_b32_e32 v53, v123
	v_mov_b32_e32 v54, v123
	v_mov_b32_e32 v55, v123
	v_mov_b32_e32 v56, v123
	v_mov_b32_e32 v57, v123
	v_mov_b32_e32 v58, v123
	v_mov_b32_e32 v59, v123
	v_mov_b32_e32 v60, v123
	v_mov_b32_e32 v61, v123
	v_mov_b32_e32 v62, v123
	v_mov_b32_e32 v63, v123
	v_mov_b32_e32 v64, v123
	v_mov_b32_e32 v65, v123
	v_mov_b32_e32 v2, v123
	v_mov_b32_e32 v3, v123
	v_mov_b32_e32 v4, v123
	v_mov_b32_e32 v5, v123
	v_mov_b32_e32 v6, v123
	v_mov_b32_e32 v7, v123
	v_mov_b32_e32 v8, v123
	v_mov_b32_e32 v9, v123
	v_mov_b32_e32 v10, v123
	v_mov_b32_e32 v11, v123
	v_mov_b32_e32 v12, v123
	v_mov_b32_e32 v13, v123
	v_mov_b32_e32 v14, v123
	v_mov_b32_e32 v15, v123
	v_mov_b32_e32 v16, v123
	v_mov_b32_e32 v17, v123
	v_mov_b32_e32 v34, v123
	v_mov_b32_e32 v35, v123
	v_mov_b32_e32 v36, v123
	v_mov_b32_e32 v37, v123
	v_mov_b32_e32 v38, v123
	v_mov_b32_e32 v39, v123
	v_mov_b32_e32 v40, v123
	v_mov_b32_e32 v41, v123
	v_mov_b32_e32 v42, v123
	v_mov_b32_e32 v43, v123
	v_mov_b32_e32 v44, v123
	v_mov_b32_e32 v45, v123
	v_mov_b32_e32 v46, v123
	v_mov_b32_e32 v47, v123
	v_mov_b32_e32 v48, v123
	v_mov_b32_e32 v49, v123
	v_add3_u32 v137, v125, v130, v131
	v_lshlrev_b32_e32 v118, 4, v134
	v_readfirstlane_b32 s52, v114
	v_readfirstlane_b32 s53, v115
	v_readfirstlane_b32 s57, v117
	v_readfirstlane_b32 s58, v121
	v_bfe_u32 v138, v134, 4, 1
	v_bfe_u32 v139, v134, 3, 1
	v_cmp_eq_u32_e32 vcc, v138, v139
	v_mov_b32_e32 v155, 0x3c003c00
	s_nop 1
	v_cndmask_b32_e32 v154, 0, v155, vcc
	v_mov_b32_e32 v122, 0
	v_mov_b32_e32 v155, v154
	v_mov_b32_e32 v156, v154
	v_mov_b32_e32 v157, v154
	v_mov_b32_e32 v123, 0
	v_mov_b32_e32 v124, 0
	v_mov_b32_e32 v125, 0
	v_mov_b32_e32 v146, 0
	v_mov_b32_e32 v147, 0
	v_mov_b32_e32 v148, 0
	v_mov_b32_e32 v149, 0
	s_mov_b32 s49, s28
	s_mul_i32 s50, s28, 48
	s_sub_i32 s50, s3, s50
	s_add_i32 s50, s50, -1
	s_mov_b32 s55, 0
	s_mov_b32 s56, 0
	s_mul_hi_u32 s59, s33, 0x2aaaaaab
	s_lshr_b32 s59, s59, 3
	s_mul_i32 s60, s59, 48
	s_sub_i32 s51, s33, s60
	s_mul_hi_u32 s60, s59, 0x2aaaaaab
	s_lshr_b32 s60, s60, 3
	s_mul_i32 s54, s60, 48
	s_sub_i32 s54, s59, s54
	s_lshl_b32 s60, s60, 2
	s_add_i32 s60, s60, s57
	s_mul_i32 s60, s60, 0xc0
	s_lshl_b32 s59, s51, 2
	s_add_i32 s60, s60, s59
	s_add_i32 s60, s60, s58
	s_lshl_b32 s60, s60, 11
	s_add_u32 s52, s52, s60
	s_addc_u32 s53, s53, 0
	s_barrier
	s_branch .LBB1_4
.LBB1_2:
	v_mov_b32_e32 v122, 0
	v_mov_b32_e32 v123, 0
	v_mov_b32_e32 v124, 0
	v_mov_b32_e32 v125, 0
	v_mov_b32_e32 v146, 0
	v_mov_b32_e32 v147, 0
	v_mov_b32_e32 v148, 0
	v_mov_b32_e32 v149, 0
	v_lshlrev_b32_e32 v118, 4, v134
	v_mov_b32_e32 v49, 0
	v_mov_b32_e32 v48, v49
	v_mov_b32_e32 v47, v49
	v_mov_b32_e32 v46, v49
	v_mov_b32_e32 v45, v49
	v_mov_b32_e32 v44, v49
	v_mov_b32_e32 v43, v49
	v_mov_b32_e32 v42, v49
	v_mov_b32_e32 v41, v49
	v_mov_b32_e32 v40, v49
	v_mov_b32_e32 v39, v49
	v_mov_b32_e32 v38, v49
	v_mov_b32_e32 v37, v49
	v_mov_b32_e32 v36, v49
	v_mov_b32_e32 v35, v49
	v_mov_b32_e32 v34, v49
	v_mov_b32_e32 v17, v49
	v_mov_b32_e32 v16, v49
	v_mov_b32_e32 v15, v49
	v_mov_b32_e32 v14, v49
	v_mov_b32_e32 v13, v49
	v_mov_b32_e32 v12, v49
	v_mov_b32_e32 v11, v49
	v_mov_b32_e32 v10, v49
	v_mov_b32_e32 v9, v49
	v_mov_b32_e32 v8, v49
	v_mov_b32_e32 v7, v49
	v_mov_b32_e32 v6, v49
	v_mov_b32_e32 v5, v49
	v_mov_b32_e32 v4, v49
	v_mov_b32_e32 v3, v49
	v_mov_b32_e32 v2, v49
	v_mov_b32_e32 v65, v49
	v_mov_b32_e32 v64, v49
	v_mov_b32_e32 v63, v49
	v_mov_b32_e32 v62, v49
	v_mov_b32_e32 v61, v49
	v_mov_b32_e32 v60, v49
	v_mov_b32_e32 v59, v49
	v_mov_b32_e32 v58, v49
	v_mov_b32_e32 v57, v49
	v_mov_b32_e32 v56, v49
	v_mov_b32_e32 v55, v49
	v_mov_b32_e32 v54, v49
	v_mov_b32_e32 v53, v49
	v_mov_b32_e32 v52, v49
	v_mov_b32_e32 v51, v49
	v_mov_b32_e32 v50, v49
	v_mov_b32_e32 v33, v49
	v_mov_b32_e32 v32, v49
	v_mov_b32_e32 v31, v49
	v_mov_b32_e32 v30, v49
	v_mov_b32_e32 v29, v49
	v_mov_b32_e32 v28, v49
	v_mov_b32_e32 v27, v49
	v_mov_b32_e32 v26, v49
	v_mov_b32_e32 v25, v49
	v_mov_b32_e32 v24, v49
	v_mov_b32_e32 v23, v49
	v_mov_b32_e32 v22, v49
	v_mov_b32_e32 v21, v49
	v_mov_b32_e32 v20, v49
	v_mov_b32_e32 v19, v49
	v_mov_b32_e32 v18, v49
	v_mov_b32_e32 v122, v49
	v_mov_b32_e32 v1, v49

.LBB1_4:
	s_add_i32 s50, s50, 1
	s_cmp_eq_u32 s50, 48
	s_cselect_b32 s50, 0, s50
	s_addc_u32 s49, s49, 0
	v_or_b32_e32 v0, s56, v129
	v_add_u32_e32 v1, s55, v137
	ds_read_b128 v[138:141], v0 offset:18432
	ds_read_b128 v[142:145], v0 offset:18448
	ds_read_b128 v[150:153], v1
	ds_read_b128 v[158:161], v1 offset:4608
	ds_read_b128 v[162:165], v1 offset:32
	ds_read_b128 v[130:133], v1 offset:4640
	global_load_dwordx4 v[110:113], v118, s[52:53]
	global_load_dwordx4 v[106:109], v118, s[52:53] offset:1024
	global_load_dwordx4 v[102:105], v118, s[52:53] offset:2048
	global_load_dwordx4 v[98:101], v118, s[52:53] offset:3072
	s_add_u32 s52, s52, 0x2000
	s_addc_u32 s53, s53, 0
	s_add_i32 s51, s51, 1
	s_cmp_lg_u32 s51, 48
	s_cbranch_scc1 .Lcb_nw0
	s_mov_b32 s51, 0
	s_sub_u32 s52, s52, 0x60000
	s_subb_u32 s53, s53, 0
	s_add_i32 s54, s54, 1
	s_cmp_lg_u32 s54, 48
	s_cbranch_scc1 .Lcb_nw0
	s_mov_b32 s54, 0
	s_add_u32 s52, s52, 0x180000
	s_addc_u32 s53, s53, 0
.Lcb_nw0:
	s_waitcnt lgkmcnt(4)
	v_pk_mul_f16 v114, v142, v136
	v_pk_mul_f16 v115, v143, v136
	v_pk_mul_f16 v166, v144, v136
	v_pk_mul_f16 v167, v145, v136
	v_pk_max_u16 v114, v114, v138
	v_pk_max_u16 v115, v115, v139
	v_pk_max_u16 v166, v166, v140
	v_pk_max_u16 v167, v167, v141
	s_waitcnt lgkmcnt(3)
	v_and_b32_e32 v150, v114, v150
	v_and_b32_e32 v151, v115, v151
	v_and_b32_e32 v152, v166, v152
	v_and_b32_e32 v153, v167, v153
	v_pk_mul_f16 v114, v142, v135
	v_pk_mul_f16 v115, v143, v135
	v_pk_mul_f16 v166, v144, v135
	v_pk_mul_f16 v167, v145, v135
	v_pk_max_u16 v114, v114, v138
	v_pk_max_u16 v115, v115, v139
	v_pk_max_u16 v166, v166, v140
	v_pk_max_u16 v167, v167, v141
	ds_read_b128 v[138:141], v0 offset:18688
	ds_read_b128 v[142:145], v0 offset:18704
	s_waitcnt lgkmcnt(4)
	v_and_b32_e32 v158, v114, v158
	v_and_b32_e32 v159, v115, v159
	v_and_b32_e32 v160, v166, v160
	v_and_b32_e32 v161, v167, v161
	s_waitcnt vmcnt(11)
	v_mfma_f32_32x32x16_f16 v[34:49], v[150:153], v[86:89], v[34:49]
	v_mfma_f32_16x16x32_f16 v[122:125], v[150:153], v[154:157], v[122:125]
	v_mfma_f32_32x32x16_f16 v[50:65], v[158:161], v[86:89], v[50:65]
	v_mfma_f32_16x16x32_f16 v[146:149], v[158:161], v[154:157], v[146:149]
	s_waitcnt vmcnt(10)
	v_mfma_f32_32x32x16_f16 v[2:17], v[150:153], v[82:85], v[2:17]
	s_waitcnt lgkmcnt(0)
	v_pk_mul_f16 v114, v142, v136
	v_pk_mul_f16 v115, v143, v136
	v_pk_mul_f16 v166, v144, v136
	v_pk_mul_f16 v167, v145, v136
	v_mfma_f32_32x32x16_f16 v[18:33], v[158:161], v[82:85], v[18:33]
	v_pk_max_u16 v114, v114, v138
	v_pk_max_u16 v115, v115, v139
	v_pk_max_u16 v166, v166, v140
	v_pk_max_u16 v167, v167, v141
	v_and_b32_e32 v162, v114, v162
	v_and_b32_e32 v163, v115, v163
	v_and_b32_e32 v164, v166, v164
	v_and_b32_e32 v165, v167, v165
	v_pk_mul_f16 v114, v142, v135
	v_pk_mul_f16 v115, v143, v135
	v_pk_mul_f16 v166, v144, v135
	v_pk_mul_f16 v167, v145, v135
	v_pk_max_u16 v114, v114, v138
	v_pk_max_u16 v115, v115, v139
	v_pk_max_u16 v166, v166, v140
	v_pk_max_u16 v167, v167, v141
	v_and_b32_e32 v130, v114, v130
	v_and_b32_e32 v131, v115, v131
	v_and_b32_e32 v132, v166, v132
	v_and_b32_e32 v133, v167, v133
	s_waitcnt vmcnt(9)
	v_mfma_f32_32x32x16_f16 v[34:49], v[162:165], v[70:73], v[34:49]
	v_mfma_f32_16x16x32_f16 v[122:125], v[162:165], v[154:157], v[122:125]
	v_mfma_f32_32x32x16_f16 v[50:65], v[130:133], v[70:73], v[50:65]
	v_mfma_f32_16x16x32_f16 v[146:149], v[130:133], v[154:157], v[146:149]
	s_waitcnt vmcnt(8)
	v_mfma_f32_32x32x16_f16 v[2:17], v[162:165], v[66:69], v[2:17]
	s_xor_b32 s55, s55, 0x2400
	s_xor_b32 s56, s56, 0x400
	v_mfma_f32_32x32x16_f16 v[18:33], v[130:133], v[66:69], v[18:33]
	s_mov_b32 s48, s49
	s_cmp_lg_u32 s50, 47
	s_barrier
	s_cbranch_scc1 .LBB1_18
	v_bfe_u32 v138, v134, 2, 2
	v_bfe_u32 v139, v134, 4, 1
	v_lshlrev_b32_e32 v138, 4, v138
	v_lshl_or_b32 v138, v139, 3, v138
	v_lshlrev_b32_e32 v138, 2, v138
	s_nop 4
	ds_bpermute_b32 v140, v138, v122
	ds_bpermute_b32 v141, v138, v123
	ds_bpermute_b32 v142, v138, v124
	ds_bpermute_b32 v143, v138, v125
	ds_bpermute_b32 v144, v138, v146
	ds_bpermute_b32 v145, v138, v147
	ds_bpermute_b32 v150, v138, v148
	ds_bpermute_b32 v151, v138, v149
	v_and_b32_e32 v139, 3, v134
	v_cmp_eq_u32_e64 s[16:17], 1, v139
	v_cmp_eq_u32_e64 s[18:19], 2, v139
	v_cmp_eq_u32_e64 s[20:21], 3, v139
	v_cmp_gt_u32_e64 s[22:23], 32, v134
	s_waitcnt lgkmcnt(0)
	v_cndmask_b32_e64 v140, v140, v141, s[16:17]
	v_cndmask_b32_e64 v144, v144, v145, s[16:17]
	v_cndmask_b32_e64 v140, v140, v142, s[18:19]
	v_cndmask_b32_e64 v144, v144, v150, s[18:19]
	v_cndmask_b32_e64 v140, v140, v143, s[20:21]
	v_cndmask_b32_e64 v144, v144, v151, s[20:21]
	v_cndmask_b32_e64 v122, 0, v140, s[22:23]
	v_cndmask_b32_e64 v1, 0, v144, s[22:23]
	v_mov_b32_e32 v123, 0
	v_mov_b32_e32 v124, v116
	v_or_b32_e32 v118, 0x2000, v116
	v_lshlrev_b32_e32 v139, 2, v119
	s_movk_i32 s16, 0x80
	v_lshl_add_u32 v138, v121, 1, v117
	v_or3_b32 v120, v139, v117, s16
	v_add_u32_e32 v126, v139, v138
	v_and_b32_e32 v66, 64, v134
	v_xor_b32_e32 v0, 32, v134
	v_add_u32_e32 v66, 64, v66
	v_cmp_lt_i32_e32 vcc, v0, v66
	s_nop 1
	v_cndmask_b32_e32 v0, v134, v0, vcc
	v_lshlrev_b32_e32 v0, 2, v0
	ds_bpermute_b32 v66, v0, v122
	ds_bpermute_b32 v0, v0, v1
	s_waitcnt lgkmcnt(1)
	v_add_f32_e32 v66, v122, v66
	s_and_saveexec_b64 s[16:17], s[6:7]
	s_xor_b64 s[16:17], exec, s[16:17]
	s_cbranch_execz .LBB1_9
	ds_write2st64_b32 v127, v34, v35 offset0:80 offset1:81
	ds_write2st64_b32 v127, v36, v37 offset0:82 offset1:83
	ds_write2st64_b32 v127, v38, v39 offset0:84 offset1:85
	ds_write2st64_b32 v127, v40, v41 offset0:86 offset1:87
	ds_write2st64_b32 v127, v42, v43 offset0:88 offset1:89
	ds_write2st64_b32 v127, v44, v45 offset0:90 offset1:91
	ds_write2st64_b32 v127, v46, v47 offset0:92 offset1:93
	ds_write2st64_b32 v127, v48, v49 offset0:94 offset1:95
	ds_write2st64_b32 v127, v2, v3 offset0:96 offset1:97
	ds_write2st64_b32 v127, v4, v5 offset0:98 offset1:99
	ds_write2st64_b32 v127, v6, v7 offset0:100 offset1:101
	ds_write2st64_b32 v127, v8, v9 offset0:102 offset1:103
	ds_write2st64_b32 v127, v10, v11 offset0:104 offset1:105
	ds_write2st64_b32 v127, v12, v13 offset0:106 offset1:107
	ds_write2st64_b32 v127, v14, v15 offset0:108 offset1:109
	ds_write2st64_b32 v127, v16, v17 offset0:110 offset1:111
	s_and_saveexec_b64 s[18:19], s[4:5]
	ds_write_b32 v128, v66
	s_or_b64 exec, exec, s[18:19]

.LBB1_17:
	s_or_b64 exec, exec, s[18:19]
	s_add_i32 s48, s48, 1
	s_mul_hi_i32 s16, s48, 0x2aaaaaab
	s_lshr_b32 s17, s16, 31
	s_ashr_i32 s16, s16, 3
	s_add_i32 s16, s16, s17
	s_mul_i32 s17, s16, 0xffffffd0
	v_lshl_or_b32 v0, s16, 2, v117
	s_add_i32 s17, s17, s48
	v_mul_lo_u32 v0, v0, s30
	v_lshl_add_u32 v0, s17, 6, v0
	v_or_b32_e32 v0, v0, v119
	v_ashrrev_i32_e32 v1, 31, v0
	v_lshl_add_u64 v[0:1], v[0:1], 1, s[8:9]
	global_load_ushort v66, v[0:1], off offset:64
	global_load_ushort v67, v[0:1], off
	v_mov_b32_e32 v49, 0
	v_mov_b32_e32 v48, v49
	v_mov_b32_e32 v47, v49
	v_mov_b32_e32 v46, v49
	v_mov_b32_e32 v45, v49
	v_mov_b32_e32 v44, v49
	v_mov_b32_e32 v43, v49
	v_mov_b32_e32 v42, v49
	v_mov_b32_e32 v41, v49
	v_mov_b32_e32 v40, v49
	v_mov_b32_e32 v39, v49
	v_mov_b32_e32 v38, v49
	v_mov_b32_e32 v37, v49
	v_mov_b32_e32 v36, v49
	v_mov_b32_e32 v35, v49
	v_mov_b32_e32 v34, v49
	v_mov_b32_e32 v17, v49
	v_mov_b32_e32 v16, v49
	v_mov_b32_e32 v15, v49
	v_mov_b32_e32 v14, v49
	v_mov_b32_e32 v13, v49
	v_mov_b32_e32 v12, v49
	v_mov_b32_e32 v11, v49
	v_mov_b32_e32 v10, v49
	v_mov_b32_e32 v9, v49
	v_mov_b32_e32 v8, v49
	v_mov_b32_e32 v7, v49
	v_mov_b32_e32 v6, v49
	v_mov_b32_e32 v5, v49
	v_mov_b32_e32 v4, v49
	v_mov_b32_e32 v3, v49
	v_mov_b32_e32 v2, v49
	v_mov_b32_e32 v65, v49
	v_mov_b32_e32 v64, v49
	v_mov_b32_e32 v63, v49
	v_mov_b32_e32 v62, v49
	v_mov_b32_e32 v61, v49
	v_mov_b32_e32 v60, v49
	v_mov_b32_e32 v59, v49
	v_mov_b32_e32 v58, v49
	v_mov_b32_e32 v57, v49
	v_mov_b32_e32 v56, v49
	v_mov_b32_e32 v55, v49
	v_mov_b32_e32 v54, v49
	v_mov_b32_e32 v53, v49
	v_mov_b32_e32 v52, v49
	v_mov_b32_e32 v51, v49
	v_mov_b32_e32 v50, v49
	v_mov_b32_e32 v33, v49
	v_mov_b32_e32 v32, v49
	v_mov_b32_e32 v31, v49
	v_mov_b32_e32 v30, v49
	v_mov_b32_e32 v29, v49
	v_mov_b32_e32 v28, v49
	v_mov_b32_e32 v27, v49
	v_mov_b32_e32 v26, v49
	v_mov_b32_e32 v25, v49
	v_mov_b32_e32 v24, v49
	v_mov_b32_e32 v23, v49
	v_mov_b32_e32 v22, v49
	v_mov_b32_e32 v21, v49
	v_mov_b32_e32 v20, v49
	v_mov_b32_e32 v19, v49
	v_mov_b32_e32 v18, v49
	v_mov_b32_e32 v122, v49
	v_mov_b32_e32 v1, v49
	s_waitcnt vmcnt(1)
	v_perm_b32 v135, v66, v66, s36
	s_waitcnt vmcnt(0)
	v_perm_b32 v136, v67, v67, s36
	v_mov_b32_e32 v122, 0
	v_mov_b32_e32 v123, 0
	v_mov_b32_e32 v124, 0
	v_mov_b32_e32 v125, 0
	v_mov_b32_e32 v146, 0
	v_mov_b32_e32 v147, 0
	v_mov_b32_e32 v148, 0
	v_mov_b32_e32 v149, 0
	v_lshlrev_b32_e32 v118, 4, v134
.LBB1_18:
	s_add_i32 s50, s50, 1
	s_cmp_eq_u32 s50, 48
	s_cselect_b32 s50, 0, s50
	s_addc_u32 s49, s49, 0
	v_or_b32_e32 v0, s56, v129
	v_add_u32_e32 v1, s55, v137
	ds_read_b128 v[138:141], v0 offset:18432
	ds_read_b128 v[142:145], v0 offset:18448
	ds_read_b128 v[150:153], v1
	ds_read_b128 v[158:161], v1 offset:4608
	ds_read_b128 v[162:165], v1 offset:32
	ds_read_b128 v[130:133], v1 offset:4640
	global_load_dwordx4 v[86:89], v118, s[52:53]
	global_load_dwordx4 v[82:85], v118, s[52:53] offset:1024
	global_load_dwordx4 v[70:73], v118, s[52:53] offset:2048
	global_load_dwordx4 v[66:69], v118, s[52:53] offset:3072
	s_add_u32 s52, s52, 0x2000
	s_addc_u32 s53, s53, 0
	s_add_i32 s51, s51, 1
	s_cmp_lg_u32 s51, 48
	s_cbranch_scc1 .Lcb_nw1
	s_mov_b32 s51, 0
	s_sub_u32 s52, s52, 0x60000
	s_subb_u32 s53, s53, 0
	s_add_i32 s54, s54, 1
	s_cmp_lg_u32 s54, 48
	s_cbranch_scc1 .Lcb_nw1
	s_mov_b32 s54, 0
	s_add_u32 s52, s52, 0x180000
	s_addc_u32 s53, s53, 0
.Lcb_nw1:
	s_waitcnt lgkmcnt(4)
	v_pk_mul_f16 v114, v142, v136
	v_pk_mul_f16 v115, v143, v136
	v_pk_mul_f16 v166, v144, v136
	v_pk_mul_f16 v167, v145, v136
	v_pk_max_u16 v114, v114, v138
	v_pk_max_u16 v115, v115, v139
	v_pk_max_u16 v166, v166, v140
	v_pk_max_u16 v167, v167, v141
	s_waitcnt lgkmcnt(3)
	v_and_b32_e32 v150, v114, v150
	v_and_b32_e32 v151, v115, v151
	v_and_b32_e32 v152, v166, v152
	v_and_b32_e32 v153, v167, v153
	v_pk_mul_f16 v114, v142, v135
	v_pk_mul_f16 v115, v143, v135
	v_pk_mul_f16 v166, v144, v135
	v_pk_mul_f16 v167, v145, v135
	v_pk_max_u16 v114, v114, v138
	v_pk_max_u16 v115, v115, v139
	v_pk_max_u16 v166, v166, v140
	v_pk_max_u16 v167, v167, v141
	ds_read_b128 v[138:141], v0 offset:18688
	ds_read_b128 v[142:145], v0 offset:18704
	s_waitcnt lgkmcnt(4)
	v_and_b32_e32 v158, v114, v158
	v_and_b32_e32 v159, v115, v159
	v_and_b32_e32 v160, v166, v160
	v_and_b32_e32 v161, v167, v161
	s_waitcnt vmcnt(11)
	v_mfma_f32_32x32x16_f16 v[34:49], v[150:153], v[94:97], v[34:49]
	v_mfma_f32_16x16x32_f16 v[122:125], v[150:153], v[154:157], v[122:125]
	v_mfma_f32_32x32x16_f16 v[50:65], v[158:161], v[94:97], v[50:65]
	v_mfma_f32_16x16x32_f16 v[146:149], v[158:161], v[154:157], v[146:149]
	s_waitcnt vmcnt(10)
	v_mfma_f32_32x32x16_f16 v[2:17], v[150:153], v[90:93], v[2:17]
	s_waitcnt lgkmcnt(0)
	v_pk_mul_f16 v114, v142, v136
	v_pk_mul_f16 v115, v143, v136
	v_pk_mul_f16 v166, v144, v136
	v_pk_mul_f16 v167, v145, v136
	v_mfma_f32_32x32x16_f16 v[18:33], v[158:161], v[90:93], v[18:33]
	v_pk_max_u16 v114, v114, v138
	v_pk_max_u16 v115, v115, v139
	v_pk_max_u16 v166, v166, v140
	v_pk_max_u16 v167, v167, v141
	v_and_b32_e32 v162, v114, v162
	v_and_b32_e32 v163, v115, v163
	v_and_b32_e32 v164, v166, v164
	v_and_b32_e32 v165, v167, v165
	v_pk_mul_f16 v114, v142, v135
	v_pk_mul_f16 v115, v143, v135
	v_pk_mul_f16 v166, v144, v135
	v_pk_mul_f16 v167, v145, v135
	v_pk_max_u16 v114, v114, v138
	v_pk_max_u16 v115, v115, v139
	v_pk_max_u16 v166, v166, v140
	v_pk_max_u16 v167, v167, v141
	v_and_b32_e32 v130, v114, v130
	v_and_b32_e32 v131, v115, v131
	v_and_b32_e32 v132, v166, v132
	v_and_b32_e32 v133, v167, v133
	s_waitcnt vmcnt(9)
	v_mfma_f32_32x32x16_f16 v[34:49], v[162:165], v[78:81], v[34:49]
	v_mfma_f32_16x16x32_f16 v[122:125], v[162:165], v[154:157], v[122:125]
	v_mfma_f32_32x32x16_f16 v[50:65], v[130:133], v[78:81], v[50:65]
	v_mfma_f32_16x16x32_f16 v[146:149], v[130:133], v[154:157], v[146:149]
	s_waitcnt vmcnt(8)
	v_mfma_f32_32x32x16_f16 v[2:17], v[162:165], v[74:77], v[2:17]
	s_xor_b32 s55, s55, 0x2400
	s_xor_b32 s56, s56, 0x400
	v_mfma_f32_32x32x16_f16 v[18:33], v[130:133], v[74:77], v[18:33]
	s_mov_b32 s47, s49
	s_cmp_lg_u32 s50, 47
	s_barrier
	s_cbranch_scc1 .LBB1_32
	v_bfe_u32 v138, v134, 2, 2
	v_bfe_u32 v139, v134, 4, 1
	v_lshlrev_b32_e32 v138, 4, v138
	v_lshl_or_b32 v138, v139, 3, v138
	v_lshlrev_b32_e32 v138, 2, v138
	s_nop 4
	ds_bpermute_b32 v140, v138, v122
	ds_bpermute_b32 v141, v138, v123
	ds_bpermute_b32 v142, v138, v124
	ds_bpermute_b32 v143, v138, v125
	ds_bpermute_b32 v144, v138, v146
	ds_bpermute_b32 v145, v138, v147
	ds_bpermute_b32 v150, v138, v148
	ds_bpermute_b32 v151, v138, v149
	v_and_b32_e32 v139, 3, v134
	v_cmp_eq_u32_e64 s[16:17], 1, v139
	v_cmp_eq_u32_e64 s[18:19], 2, v139
	v_cmp_eq_u32_e64 s[20:21], 3, v139
	v_cmp_gt_u32_e64 s[22:23], 32, v134
	s_waitcnt lgkmcnt(0)
	v_cndmask_b32_e64 v140, v140, v141, s[16:17]
	v_cndmask_b32_e64 v144, v144, v145, s[16:17]
	v_cndmask_b32_e64 v140, v140, v142, s[18:19]
	v_cndmask_b32_e64 v144, v144, v150, s[18:19]
	v_cndmask_b32_e64 v140, v140, v143, s[20:21]
	v_cndmask_b32_e64 v144, v144, v151, s[20:21]
	v_cndmask_b32_e64 v122, 0, v140, s[22:23]
	v_cndmask_b32_e64 v1, 0, v144, s[22:23]
	v_mov_b32_e32 v123, 0
	v_mov_b32_e32 v124, v116
	v_or_b32_e32 v118, 0x2000, v116
	v_lshlrev_b32_e32 v139, 2, v119
	s_movk_i32 s16, 0x80
	v_lshl_add_u32 v138, v121, 1, v117
	v_or3_b32 v120, v139, v117, s16
	v_add_u32_e32 v126, v139, v138
	v_and_b32_e32 v74, 64, v134
	v_xor_b32_e32 v0, 32, v134
	v_add_u32_e32 v74, 64, v74
	v_cmp_lt_i32_e32 vcc, v0, v74
	s_nop 1
	v_cndmask_b32_e32 v0, v134, v0, vcc
	v_lshlrev_b32_e32 v0, 2, v0
	ds_bpermute_b32 v74, v0, v122
	ds_bpermute_b32 v0, v0, v1
	s_waitcnt lgkmcnt(1)
	v_add_f32_e32 v74, v122, v74
	s_and_saveexec_b64 s[16:17], s[6:7]
	s_xor_b64 s[16:17], exec, s[16:17]
	s_cbranch_execz .LBB1_23
	ds_write2st64_b32 v127, v34, v35 offset0:80 offset1:81
	ds_write2st64_b32 v127, v36, v37 offset0:82 offset1:83
	ds_write2st64_b32 v127, v38, v39 offset0:84 offset1:85
	ds_write2st64_b32 v127, v40, v41 offset0:86 offset1:87
	ds_write2st64_b32 v127, v42, v43 offset0:88 offset1:89
	ds_write2st64_b32 v127, v44, v45 offset0:90 offset1:91
	ds_write2st64_b32 v127, v46, v47 offset0:92 offset1:93
	ds_write2st64_b32 v127, v48, v49 offset0:94 offset1:95
	ds_write2st64_b32 v127, v2, v3 offset0:96 offset1:97
	ds_write2st64_b32 v127, v4, v5 offset0:98 offset1:99
	ds_write2st64_b32 v127, v6, v7 offset0:100 offset1:101
	ds_write2st64_b32 v127, v8, v9 offset0:102 offset1:103
	ds_write2st64_b32 v127, v10, v11 offset0:104 offset1:105
	ds_write2st64_b32 v127, v12, v13 offset0:106 offset1:107
	ds_write2st64_b32 v127, v14, v15 offset0:108 offset1:109
	ds_write2st64_b32 v127, v16, v17 offset0:110 offset1:111
	s_and_saveexec_b64 s[18:19], s[4:5]
	ds_write_b32 v128, v74
	s_or_b64 exec, exec, s[18:19]

.LBB1_31:
	s_or_b64 exec, exec, s[18:19]
	s_add_i32 s47, s47, 1
	s_mul_hi_i32 s16, s47, 0x2aaaaaab
	s_lshr_b32 s17, s16, 31
	s_ashr_i32 s16, s16, 3
	s_add_i32 s16, s16, s17
	s_mul_i32 s17, s16, 0xffffffd0
	v_lshl_or_b32 v0, s16, 2, v117
	s_add_i32 s17, s17, s47
	v_mul_lo_u32 v0, v0, s30
	v_lshl_add_u32 v0, s17, 6, v0
	v_or_b32_e32 v0, v0, v119
	v_ashrrev_i32_e32 v1, 31, v0
	v_lshl_add_u64 v[0:1], v[0:1], 1, s[8:9]
	global_load_ushort v74, v[0:1], off offset:64
	global_load_ushort v75, v[0:1], off
	v_mov_b32_e32 v49, 0
	v_mov_b32_e32 v48, v49
	v_mov_b32_e32 v47, v49
	v_mov_b32_e32 v46, v49
	v_mov_b32_e32 v45, v49
	v_mov_b32_e32 v44, v49
	v_mov_b32_e32 v43, v49
	v_mov_b32_e32 v42, v49
	v_mov_b32_e32 v41, v49
	v_mov_b32_e32 v40, v49
	v_mov_b32_e32 v39, v49
	v_mov_b32_e32 v38, v49
	v_mov_b32_e32 v37, v49
	v_mov_b32_e32 v36, v49
	v_mov_b32_e32 v35, v49
	v_mov_b32_e32 v34, v49
	v_mov_b32_e32 v17, v49
	v_mov_b32_e32 v16, v49
	v_mov_b32_e32 v15, v49
	v_mov_b32_e32 v14, v49
	v_mov_b32_e32 v13, v49
	v_mov_b32_e32 v12, v49
	v_mov_b32_e32 v11, v49
	v_mov_b32_e32 v10, v49
	v_mov_b32_e32 v9, v49
	v_mov_b32_e32 v8, v49
	v_mov_b32_e32 v7, v49
	v_mov_b32_e32 v6, v49
	v_mov_b32_e32 v5, v49
	v_mov_b32_e32 v4, v49
	v_mov_b32_e32 v3, v49
	v_mov_b32_e32 v2, v49
	v_mov_b32_e32 v65, v49
	v_mov_b32_e32 v64, v49
	v_mov_b32_e32 v63, v49
	v_mov_b32_e32 v62, v49
	v_mov_b32_e32 v61, v49
	v_mov_b32_e32 v60, v49
	v_mov_b32_e32 v59, v49
	v_mov_b32_e32 v58, v49
	v_mov_b32_e32 v57, v49
	v_mov_b32_e32 v56, v49
	v_mov_b32_e32 v55, v49
	v_mov_b32_e32 v54, v49
	v_mov_b32_e32 v53, v49
	v_mov_b32_e32 v52, v49
	v_mov_b32_e32 v51, v49
	v_mov_b32_e32 v50, v49
	v_mov_b32_e32 v33, v49
	v_mov_b32_e32 v32, v49
	v_mov_b32_e32 v31, v49
	v_mov_b32_e32 v30, v49
	v_mov_b32_e32 v29, v49
	v_mov_b32_e32 v28, v49
	v_mov_b32_e32 v27, v49
	v_mov_b32_e32 v26, v49
	v_mov_b32_e32 v25, v49
	v_mov_b32_e32 v24, v49
	v_mov_b32_e32 v23, v49
	v_mov_b32_e32 v22, v49
	v_mov_b32_e32 v21, v49
	v_mov_b32_e32 v20, v49
	v_mov_b32_e32 v19, v49
	v_mov_b32_e32 v18, v49
	v_mov_b32_e32 v122, v49
	v_mov_b32_e32 v1, v49
	s_waitcnt vmcnt(1)
	v_perm_b32 v135, v74, v74, s36
	s_waitcnt vmcnt(0)
	v_perm_b32 v136, v75, v75, s36
	v_mov_b32_e32 v122, 0
	v_mov_b32_e32 v123, 0
	v_mov_b32_e32 v124, 0
	v_mov_b32_e32 v125, 0
	v_mov_b32_e32 v146, 0
	v_mov_b32_e32 v147, 0
	v_mov_b32_e32 v148, 0
	v_mov_b32_e32 v149, 0
	v_lshlrev_b32_e32 v118, 4, v134
.LBB1_32:
	s_add_i32 s50, s50, 1
	s_cmp_eq_u32 s50, 48
	s_cselect_b32 s50, 0, s50
	s_addc_u32 s49, s49, 0
	v_or_b32_e32 v0, s56, v129
	v_add_u32_e32 v1, s55, v137
	ds_read_b128 v[138:141], v0 offset:18432
	ds_read_b128 v[142:145], v0 offset:18448
	ds_read_b128 v[150:153], v1
	ds_read_b128 v[158:161], v1 offset:4608
	ds_read_b128 v[162:165], v1 offset:32
	ds_read_b128 v[130:133], v1 offset:4640
	global_load_dwordx4 v[94:97], v118, s[52:53]
	global_load_dwordx4 v[90:93], v118, s[52:53] offset:1024
	global_load_dwordx4 v[78:81], v118, s[52:53] offset:2048
	global_load_dwordx4 v[74:77], v118, s[52:53] offset:3072
	s_add_u32 s52, s52, 0x2000
	s_addc_u32 s53, s53, 0
	s_add_i32 s51, s51, 1
	s_cmp_lg_u32 s51, 48
	s_cbranch_scc1 .Lcb_nw2
	s_mov_b32 s51, 0
	s_sub_u32 s52, s52, 0x60000
	s_subb_u32 s53, s53, 0
	s_add_i32 s54, s54, 1
	s_cmp_lg_u32 s54, 48
	s_cbranch_scc1 .Lcb_nw2
	s_mov_b32 s54, 0
	s_add_u32 s52, s52, 0x180000
	s_addc_u32 s53, s53, 0
.Lcb_nw2:
	s_waitcnt lgkmcnt(4)
	v_pk_mul_f16 v114, v142, v136
	v_pk_mul_f16 v115, v143, v136
	v_pk_mul_f16 v166, v144, v136
	v_pk_mul_f16 v167, v145, v136
	v_pk_max_u16 v114, v114, v138
	v_pk_max_u16 v115, v115, v139
	v_pk_max_u16 v166, v166, v140
	v_pk_max_u16 v167, v167, v141
	s_waitcnt lgkmcnt(3)
	v_and_b32_e32 v150, v114, v150
	v_and_b32_e32 v151, v115, v151
	v_and_b32_e32 v152, v166, v152
	v_and_b32_e32 v153, v167, v153
	v_pk_mul_f16 v114, v142, v135
	v_pk_mul_f16 v115, v143, v135
	v_pk_mul_f16 v166, v144, v135
	v_pk_mul_f16 v167, v145, v135
	v_pk_max_u16 v114, v114, v138
	v_pk_max_u16 v115, v115, v139
	v_pk_max_u16 v166, v166, v140
	v_pk_max_u16 v167, v167, v141
	ds_read_b128 v[138:141], v0 offset:18688
	ds_read_b128 v[142:145], v0 offset:18704
	s_waitcnt lgkmcnt(4)
	v_and_b32_e32 v158, v114, v158
	v_and_b32_e32 v159, v115, v159
	v_and_b32_e32 v160, v166, v160
	v_and_b32_e32 v161, v167, v161
	s_waitcnt vmcnt(11)
	v_mfma_f32_32x32x16_f16 v[34:49], v[150:153], v[110:113], v[34:49]
	v_mfma_f32_16x16x32_f16 v[122:125], v[150:153], v[154:157], v[122:125]
	v_mfma_f32_32x32x16_f16 v[50:65], v[158:161], v[110:113], v[50:65]
	v_mfma_f32_16x16x32_f16 v[146:149], v[158:161], v[154:157], v[146:149]
	s_waitcnt vmcnt(10)
	v_mfma_f32_32x32x16_f16 v[2:17], v[150:153], v[106:109], v[2:17]
	s_waitcnt lgkmcnt(0)
	v_pk_mul_f16 v114, v142, v136
	v_pk_mul_f16 v115, v143, v136
	v_pk_mul_f16 v166, v144, v136
	v_pk_mul_f16 v167, v145, v136
	v_mfma_f32_32x32x16_f16 v[18:33], v[158:161], v[106:109], v[18:33]
	v_pk_max_u16 v114, v114, v138
	v_pk_max_u16 v115, v115, v139
	v_pk_max_u16 v166, v166, v140
	v_pk_max_u16 v167, v167, v141
	v_and_b32_e32 v162, v114, v162
	v_and_b32_e32 v163, v115, v163
	v_and_b32_e32 v164, v166, v164
	v_and_b32_e32 v165, v167, v165
	v_pk_mul_f16 v114, v142, v135
	v_pk_mul_f16 v115, v143, v135
	v_pk_mul_f16 v166, v144, v135
	v_pk_mul_f16 v167, v145, v135
	v_pk_max_u16 v114, v114, v138
	v_pk_max_u16 v115, v115, v139
	v_pk_max_u16 v166, v166, v140
	v_pk_max_u16 v167, v167, v141
	v_and_b32_e32 v130, v114, v130
	v_and_b32_e32 v131, v115, v131
	v_and_b32_e32 v132, v166, v132
	v_and_b32_e32 v133, v167, v133
	s_waitcnt vmcnt(9)
	v_mfma_f32_32x32x16_f16 v[34:49], v[162:165], v[102:105], v[34:49]
	v_mfma_f32_16x16x32_f16 v[122:125], v[162:165], v[154:157], v[122:125]
	v_mfma_f32_32x32x16_f16 v[50:65], v[130:133], v[102:105], v[50:65]
	v_mfma_f32_16x16x32_f16 v[146:149], v[130:133], v[154:157], v[146:149]
	s_waitcnt vmcnt(8)
	v_mfma_f32_32x32x16_f16 v[2:17], v[162:165], v[98:101], v[2:17]
	s_xor_b32 s55, s55, 0x2400
	s_xor_b32 s56, s56, 0x400
	v_mfma_f32_32x32x16_f16 v[18:33], v[130:133], v[98:101], v[18:33]
	s_mov_b32 s44, s49
	s_cmp_eq_u32 s50, 47
	s_cselect_b32 s16, 1, 0
	s_cmp_eq_u32 s42, 24
	s_cselect_b32 s17, 1, 0
	s_or_b32 s16, s16, s17
	s_barrier
	s_cbranch_scc0 .LBB1_3
	v_bfe_u32 v138, v134, 2, 2
	v_bfe_u32 v139, v134, 4, 1
	v_lshlrev_b32_e32 v138, 4, v138
	v_lshl_or_b32 v138, v139, 3, v138
	v_lshlrev_b32_e32 v138, 2, v138
	s_nop 4
	ds_bpermute_b32 v140, v138, v122
	ds_bpermute_b32 v141, v138, v123
	ds_bpermute_b32 v142, v138, v124
	ds_bpermute_b32 v143, v138, v125
	ds_bpermute_b32 v144, v138, v146
	ds_bpermute_b32 v145, v138, v147
	ds_bpermute_b32 v150, v138, v148
	ds_bpermute_b32 v151, v138, v149
	v_and_b32_e32 v139, 3, v134
	v_cmp_eq_u32_e64 s[16:17], 1, v139
	v_cmp_eq_u32_e64 s[18:19], 2, v139
	v_cmp_eq_u32_e64 s[20:21], 3, v139
	v_cmp_gt_u32_e64 s[22:23], 32, v134
	s_waitcnt lgkmcnt(0)
	v_cndmask_b32_e64 v140, v140, v141, s[16:17]
	v_cndmask_b32_e64 v144, v144, v145, s[16:17]
	v_cndmask_b32_e64 v140, v140, v142, s[18:19]
	v_cndmask_b32_e64 v144, v144, v150, s[18:19]
	v_cndmask_b32_e64 v140, v140, v143, s[20:21]
	v_cndmask_b32_e64 v144, v144, v151, s[20:21]
	v_cndmask_b32_e64 v122, 0, v140, s[22:23]
	v_cndmask_b32_e64 v1, 0, v144, s[22:23]
	v_mov_b32_e32 v123, 0
	v_mov_b32_e32 v124, v116
	v_or_b32_e32 v118, 0x2000, v116
	v_lshlrev_b32_e32 v139, 2, v119
	s_movk_i32 s16, 0x80
	v_lshl_add_u32 v138, v121, 1, v117
	v_or3_b32 v120, v139, v117, s16
	v_add_u32_e32 v126, v139, v138
	v_and_b32_e32 v98, 64, v134
	v_xor_b32_e32 v0, 32, v134
	v_add_u32_e32 v98, 64, v98
	v_cmp_lt_i32_e32 vcc, v0, v98
	s_nop 1
	v_cndmask_b32_e32 v0, v134, v0, vcc
	v_lshlrev_b32_e32 v0, 2, v0
	ds_bpermute_b32 v98, v0, v122
	ds_bpermute_b32 v0, v0, v1
	s_waitcnt lgkmcnt(1)
	v_add_f32_e32 v98, v122, v98
	s_and_saveexec_b64 s[16:17], s[6:7]
	s_xor_b64 s[16:17], exec, s[16:17]
	s_cbranch_execz .LBB1_37
	ds_write2st64_b32 v127, v34, v35 offset0:80 offset1:81
	ds_write2st64_b32 v127, v36, v37 offset0:82 offset1:83
	ds_write2st64_b32 v127, v38, v39 offset0:84 offset1:85
	ds_write2st64_b32 v127, v40, v41 offset0:86 offset1:87
	ds_write2st64_b32 v127, v42, v43 offset0:88 offset1:89
	ds_write2st64_b32 v127, v44, v45 offset0:90 offset1:91
	ds_write2st64_b32 v127, v46, v47 offset0:92 offset1:93
	ds_write2st64_b32 v127, v48, v49 offset0:94 offset1:95
	ds_write2st64_b32 v127, v2, v3 offset0:96 offset1:97
	ds_write2st64_b32 v127, v4, v5 offset0:98 offset1:99
	ds_write2st64_b32 v127, v6, v7 offset0:100 offset1:101
	ds_write2st64_b32 v127, v8, v9 offset0:102 offset1:103
	ds_write2st64_b32 v127, v10, v11 offset0:104 offset1:105
	ds_write2st64_b32 v127, v12, v13 offset0:106 offset1:107
	ds_write2st64_b32 v127, v14, v15 offset0:108 offset1:109
	ds_write2st64_b32 v127, v16, v17 offset0:110 offset1:111
	s_and_saveexec_b64 s[18:19], s[4:5]
	ds_write_b32 v128, v98
	s_or_b64 exec, exec, s[18:19]

	.amdhsa_kernel _Z11attn_kernelPKiPKDv8_DF16_PKDF16_S5_PDF16_Pf
		.amdhsa_group_segment_fixed_size 87040
		.amdhsa_private_segment_fixed_size 0
		.amdhsa_kernarg_size 48
		.amdhsa_user_sgpr_count 2
		.amdhsa_user_sgpr_dispatch_ptr 0
		.amdhsa_user_sgpr_queue_ptr 0
		.amdhsa_user_sgpr_kernarg_segment_ptr 1
		.amdhsa_user_sgpr_dispatch_id 0
		.amdhsa_user_sgpr_kernarg_preload_length 0
		.amdhsa_user_sgpr_kernarg_preload_offset 0
		.amdhsa_user_sgpr_private_segment_size 0
		.amdhsa_uses_dynamic_stack 0
		.amdhsa_enable_private_segment 0
		.amdhsa_system_sgpr_workgroup_id_x 1
		.amdhsa_system_sgpr_workgroup_id_y 0
		.amdhsa_system_sgpr_workgroup_id_z 0
		.amdhsa_system_sgpr_workgroup_info 0
		.amdhsa_system_vgpr_workitem_id 0
		.amdhsa_next_free_vgpr 168
		.amdhsa_next_free_sgpr 96
		.amdhsa_accum_offset 168
		.amdhsa_reserve_vcc 1
		.amdhsa_float_round_mode_32 0
		.amdhsa_float_round_mode_16_64 0
		.amdhsa_float_denorm_mode_32 3
		.amdhsa_float_denorm_mode_16_64 3
		.amdhsa_dx10_clamp 1
		.amdhsa_ieee_mode 1
		.amdhsa_fp16_overflow 0
		.amdhsa_tg_split 0
		.amdhsa_exception_fp_ieee_invalid_op 0
		.amdhsa_exception_fp_denorm_src 0
		.amdhsa_exception_fp_ieee_div_zero 0
		.amdhsa_exception_fp_ieee_overflow 0
		.amdhsa_exception_fp_ieee_underflow 0
		.amdhsa_exception_fp_ieee_inexact 0
		.amdhsa_exception_int_div_zero 0
	.end_amdhsa_kernel

amdhsa.kernels:
  - .agpr_count:     0
    .args:
      - .actual_access:  read_only
        .address_space:  global
        .offset:         0
        .size:           8
        .value_kind:     global_buffer
      - .actual_access:  read_only
        .address_space:  global
        .offset:         8
        .size:           8
        .value_kind:     global_buffer
      - .actual_access:  read_only
        .address_space:  global
        .offset:         16
        .size:           8
        .value_kind:     global_buffer
      - .actual_access:  write_only
        .address_space:  global
        .offset:         24
        .size:           8
        .value_kind:     global_buffer
      - .actual_access:  write_only
        .address_space:  global
        .offset:         32
        .size:           8
        .value_kind:     global_buffer
      - .actual_access:  write_only
        .address_space:  global
        .offset:         40
        .size:           8
        .value_kind:     global_buffer
    .group_segment_fixed_size: 57344
    .kernarg_segment_align: 8
    .kernarg_segment_size: 48
    .language:       OpenCL C
    .language_version:
      - 2
      - 0
    .max_flat_workgroup_size: 512
    .name:           _Z12gemm1_kernelPKfS0_S0_PDv8_DF16_PDF16_S3_
    .private_segment_fixed_size: 0
    .sgpr_count:     18
    .sgpr_spill_count: 0
    .symbol:         _Z12gemm1_kernelPKfS0_S0_PDv8_DF16_PDF16_S3_.kd
    .uniform_work_group_size: 1
    .uses_dynamic_stack: false
    .vgpr_count:     125
    .vgpr_spill_count: 0
    .wavefront_size: 64
  - .agpr_count:     0
    .args:
      - .actual_access:  read_only
        .address_space:  global
        .offset:         0
        .size:           8
        .value_kind:     global_buffer
      - .actual_access:  read_only
        .address_space:  global
        .offset:         8
        .size:           8
        .value_kind:     global_buffer
      - .actual_access:  read_only
        .address_space:  global
        .offset:         16
        .size:           8
        .value_kind:     global_buffer
      - .actual_access:  read_only
        .address_space:  global
        .offset:         24
        .size:           8
        .value_kind:     global_buffer
      - .actual_access:  write_only
        .address_space:  global
        .offset:         32
        .size:           8
        .value_kind:     global_buffer
      - .actual_access:  write_only
        .address_space:  global
        .offset:         40
        .size:           8
        .value_kind:     global_buffer
    .group_segment_fixed_size: 87040
    .kernarg_segment_align: 8
    .kernarg_segment_size: 48
    .language:       OpenCL C
    .language_version:
      - 2
      - 0
    .max_flat_workgroup_size: 768
    .name:           _Z11attn_kernelPKiPKDv8_DF16_PKDF16_S5_PDF16_Pf
    .private_segment_fixed_size: 0
    .sgpr_count:     55
    .sgpr_spill_count: 0
    .symbol:         _Z11attn_kernelPKiPKDv8_DF16_PKDF16_S5_PDF16_Pf.kd
    .uniform_work_group_size: 1
    .uses_dynamic_stack: false
    .vgpr_count:     168
    .vgpr_spill_count: 0
    .wavefront_size: 64
  - .agpr_count:     12
    .args:
      - .actual_access:  read_only
        .address_space:  global
        .offset:         0
        .size:           8
        .value_kind:     global_buffer
      - .actual_access:  read_only
        .address_space:  global
        .offset:         8
        .size:           8
        .value_kind:     global_buffer
      - .actual_access:  read_only
        .address_space:  global
        .offset:         16
        .size:           8
        .value_kind:     global_buffer
      - .actual_access:  read_only
        .address_space:  global
        .offset:         24
        .size:           8
        .value_kind:     global_buffer
      - .actual_access:  read_only
        .address_space:  global
        .offset:         32
        .size:           8
        .value_kind:     global_buffer
      - .actual_access:  read_only
        .address_space:  global
        .offset:         40
        .size:           8
        .value_kind:     global_buffer
      - .actual_access:  write_only
        .address_space:  global
        .offset:         48
        .size:           8
        .value_kind:     global_buffer
    .group_segment_fixed_size: 16192
    .kernarg_segment_align: 8
    .kernarg_segment_size: 56
    .language:       OpenCL C
    .language_version:
      - 2
      - 0
    .max_flat_workgroup_size: 256
    .name:           _Z10epi_kernelPKDF16_PKfS2_S2_S2_S2_Pf
    .private_segment_fixed_size: 0
    .sgpr_count:     24
    .sgpr_spill_count: 0
    .symbol:         _Z10epi_kernelPKDF16_PKfS2_S2_S2_S2_Pf.kd
    .uniform_work_group_size: 1
    .uses_dynamic_stack: false
    .vgpr_count:     124
    .vgpr_spill_count: 0
    .wavefront_size: 64
